# v10 + final output stores without the nt hint (plain write-back stores merge half lines in L2)
# speedup vs baseline: 1.0081x; 1.0054x over previous
; #define GAS __attribute__((address_space(1)))
;     ...
;         if constexpr (ES == 1) asm volatile("s_nop 15\n\ts_nop 15" ::: "memory");
;     __device__ __forceinline__ void operator()(const f32x4 (&acc)[2][2][4][2], const Unit& u, int wr, int wc, int fr, int fq) const {
;         const int row0 = u.pm * 256 + wr * 64 + fr, col0 = u.pn * 256 + wc * 32 + 4 * fq; const float* gp = gate + (u.pm >> 3) * MODW + col0;
;         f32x4 gv[2][2];
; #pragma unroll
;         for (int bj = 0; bj < 2; ++bj)
; #pragma unroll
;             for (int n = 0; n < 2; ++n) gv[bj][n] = *(const GAS f32x4*)(gp + bj * 128 + n * 16) * scale;
;         size_t off0 = (size_t)row0 * DM + col0; asm volatile("" : "+v"(off0));
;         f32x4 B0[4], B1[4];
;     ...
;         ER_LOAD(B0, 0); ER_LOAD(B1, 1); ER_STORE(B0, 0); ER_LOAD(B0, 2); ER_STORE(B1, 1); ER_LOAD(B1, 3); ER_STORE(B0, 2); ER_LOAD(B0, 4); ER_STORE(B1, 3); ER_LOAD(B1, 5);
.LBB0_2651:
	s_lshr_b32 s44, s79, 3
	s_mulk_i32 s44, 0x6000
	s_ashr_i32 s45, s44, 31
	s_lshl_b64 s[44:45], s[44:45], 2
	v_lshl_or_b32 v0, s80, 8, v182
	s_add_u32 s44, s57, s44
	s_addc_u32 s45, s58, s45
	v_ashrrev_i32_e32 v1, 31, v0
	s_nop 15
	s_nop 15
	v_lshl_add_u64 v[10:11], v[0:1], 2, s[44:45]
	global_load_dwordx4 v[2:5], v[10:11], off
	global_load_dwordx4 v[6:9], v[10:11], off offset:64
	global_load_dwordx4 v[20:23], v[10:11], off offset:512
	global_load_dwordx4 v[24:27], v[10:11], off offset:576
	v_lshl_add_u32 v10, s79, 8, v180
	v_ashrrev_i32_e32 v11, 31, v10
	v_lshlrev_b64 v[10:11], 12, v[10:11]
	v_readlane_b32 s44, v248, 6
	v_lshl_add_u64 v[0:1], v[10:11], 0, v[0:1]
	v_readlane_b32 s45, v248, 7
	v_readlane_b32 s92, v248, 14
	v_readlane_b32 s89, v248, 15
	v_lshl_add_u64 v[18:19], v[0:1], 1, s[44:45]
	v_add_co_u32_e32 v10, vcc, s64, v18
	global_load_dwordx2 v[28:29], v[18:19], off
	global_load_dwordx2 v[30:31], v[18:19], off offset:32
	global_load_dwordx2 v[172:173], v[18:19], off offset:256
	global_load_dwordx2 v[174:175], v[18:19], off offset:288
	v_addc_co_u32_e32 v11, vcc, 0, v19, vcc
	global_load_dwordx2 v[176:177], v[10:11], off
	v_lshl_add_u64 v[10:11], v[18:19], 0, s[14:15]
	global_load_dwordx2 v[178:179], v[10:11], off offset:32
	global_load_dwordx2 v[186:187], v[10:11], off offset:256
	global_load_dwordx2 v[188:189], v[10:11], off offset:288
	v_readlane_b32 s44, v249, 0
	v_readlane_b32 s50, v249, 6
	v_readlane_b32 s51, v249, 7
	v_add_co_u32_e32 v192, vcc, s65, v18
	s_nop 0
	v_lshl_add_u64 v[0:1], v[0:1], 2, s[50:51]
	v_addc_co_u32_e32 v193, vcc, 0, v19, vcc
	v_lshl_add_u64 v[190:191], v[18:19], 0, s[16:17]
	v_readlane_b32 s45, v249, 1
	v_readlane_b32 s46, v249, 2
	v_readlane_b32 s47, v249, 3
	v_readlane_b32 s48, v249, 4
	v_readlane_b32 s49, v249, 5
	s_waitcnt vmcnt(0)
	v_pk_mul_f32 v[14:15], v[4:5], s[12:13] op_sel_hi:[1,0]
	v_pk_mul_f32 v[16:17], v[2:3], s[12:13] op_sel_hi:[1,0]
	v_pk_mul_f32 v[12:13], v[8:9], s[12:13] op_sel_hi:[1,0]
	v_pk_mul_f32 v[10:11], v[6:7], s[12:13] op_sel_hi:[1,0]
	v_pk_mul_f32 v[8:9], v[22:23], s[12:13] op_sel_hi:[1,0]
	v_pk_mul_f32 v[6:7], v[20:21], s[12:13] op_sel_hi:[1,0]
	v_pk_mul_f32 v[4:5], v[26:27], s[12:13] op_sel_hi:[1,0]
	v_pk_mul_f32 v[2:3], v[24:25], s[12:13] op_sel_hi:[1,0]
	v_lshlrev_b32_e32 v20, 16, v28
	v_and_b32_e32 v21, 0xffff0000, v28
	v_lshlrev_b32_e32 v22, 16, v29
	v_and_b32_e32 v23, 0xffff0000, v29
	v_lshlrev_b32_e32 v24, 16, v30
	v_and_b32_e32 v25, 0xffff0000, v30
	v_lshlrev_b32_e32 v26, 16, v31
	v_and_b32_e32 v27, 0xffff0000, v31
	v_lshlrev_b32_e32 v28, 16, v172
	v_and_b32_e32 v29, 0xffff0000, v172
	v_lshlrev_b32_e32 v30, 16, v173
	v_and_b32_e32 v31, 0xffff0000, v173
	v_lshlrev_b32_e32 v172, 16, v174
	v_and_b32_e32 v173, 0xffff0000, v174
	v_lshlrev_b32_e32 v174, 16, v175
	v_and_b32_e32 v175, 0xffff0000, v175
	v_lshlrev_b32_e32 v194, 16, v176
	v_and_b32_e32 v195, 0xffff0000, v176
	v_lshlrev_b32_e32 v176, 16, v177
	v_and_b32_e32 v177, 0xffff0000, v177
	v_pk_fma_f32 v[22:23], v[158:159], v[14:15], v[22:23]
	v_pk_fma_f32 v[20:21], v[156:157], v[16:17], v[20:21]
	v_pk_fma_f32 v[26:27], v[154:155], v[12:13], v[26:27]
	v_pk_fma_f32 v[24:25], v[152:153], v[10:11], v[24:25]
	v_pk_fma_f32 v[30:31], v[150:151], v[8:9], v[30:31]
	v_pk_fma_f32 v[28:29], v[148:149], v[6:7], v[28:29]
	v_pk_fma_f32 v[146:147], v[146:147], v[4:5], v[174:175]
	v_pk_fma_f32 v[144:145], v[144:145], v[2:3], v[172:173]
	global_store_dwordx4 v[0:1], v[20:23], off
	global_store_dwordx4 v[0:1], v[24:27], off offset:64
	global_store_dwordx4 v[0:1], v[28:31], off offset:512
	global_store_dwordx4 v[0:1], v[144:147], off offset:576
	v_pk_fma_f32 v[22:23], v[142:143], v[14:15], v[176:177]
	v_add_co_u32_e32 v142, vcc, s65, v0
	v_lshlrev_b32_e32 v196, 16, v178
	v_and_b32_e32 v197, 0xffff0000, v178
	v_lshlrev_b32_e32 v178, 16, v179
	v_and_b32_e32 v179, 0xffff0000, v179
	v_pk_fma_f32 v[20:21], v[140:141], v[16:17], v[194:195]
	v_addc_co_u32_e32 v143, vcc, 0, v1, vcc
	v_lshlrev_b32_e32 v198, 16, v186
	v_and_b32_e32 v199, 0xffff0000, v186
	v_lshlrev_b32_e32 v186, 16, v187
	v_and_b32_e32 v187, 0xffff0000, v187
	global_load_dwordx2 v[24:25], v[192:193], off
	global_load_dwordx2 v[26:27], v[190:191], off offset:32
	global_load_dwordx2 v[28:29], v[190:191], off offset:256
	global_load_dwordx2 v[30:31], v[190:191], off offset:288
	v_lshl_add_u64 v[140:141], v[0:1], 0, s[16:17]
	global_store_dwordx4 v[142:143], v[20:23], off
	v_lshlrev_b32_e32 v200, 16, v188
	v_and_b32_e32 v201, 0xffff0000, v188
	v_pk_fma_f32 v[22:23], v[138:139], v[12:13], v[178:179]
	v_pk_fma_f32 v[20:21], v[136:137], v[10:11], v[196:197]
	v_lshlrev_b32_e32 v188, 16, v189
	v_and_b32_e32 v189, 0xffff0000, v189
	global_store_dwordx4 v[140:141], v[20:23], off offset:64
	v_lshl_add_u64 v[136:137], v[18:19], 0, s[22:23]
	s_waitcnt vmcnt(4)
	v_lshlrev_b32_e32 v142, 16, v26
	v_pk_fma_f32 v[22:23], v[134:135], v[8:9], v[186:187]
	v_pk_fma_f32 v[20:21], v[132:133], v[6:7], v[198:199]
	global_store_dwordx4 v[140:141], v[20:23], off offset:512
	v_and_b32_e32 v143, 0xffff0000, v26
	v_lshlrev_b32_e32 v26, 16, v27
	v_pk_fma_f32 v[22:23], v[130:131], v[4:5], v[188:189]
	v_pk_fma_f32 v[20:21], v[128:129], v[2:3], v[200:201]
	global_store_dwordx4 v[140:141], v[20:23], off offset:576
	v_lshlrev_b32_e32 v140, 16, v24
	v_and_b32_e32 v141, 0xffff0000, v24
	v_add_co_u32_e32 v20, vcc, s66, v18
	v_lshl_add_u64 v[22:23], v[18:19], 0, s[18:19]
	s_nop 0
	v_addc_co_u32_e32 v21, vcc, 0, v19, vcc
	global_load_dwordx2 v[20:21], v[20:21], off
	s_nop 0
	global_load_dwordx2 v[128:129], v[22:23], off offset:32
	global_load_dwordx2 v[130:131], v[22:23], off offset:256
	s_nop 0
	global_load_dwordx2 v[22:23], v[22:23], off offset:288
	v_add_co_u32_e32 v134, vcc, s67, v0
	v_lshlrev_b32_e32 v24, 16, v25
	s_nop 0
	v_addc_co_u32_e32 v135, vcc, 0, v1, vcc
	v_add_co_u32_e32 v138, vcc, s68, v18
	v_and_b32_e32 v25, 0xffff0000, v25
	s_nop 0
	v_addc_co_u32_e32 v139, vcc, 0, v19, vcc
	v_and_b32_e32 v27, 0xffff0000, v27
	s_waitcnt vmcnt(9)
;     __device__ __forceinline__ void operator()(const f32x4 (&acc)[2][2][4][2], const Unit& u, int wr, int wc, int fr, int fq) const {
;     ...
;         ER_LOAD(B0, 0); ER_LOAD(B1, 1); ER_STORE(B0, 0); ER_LOAD(B0, 2); ER_STORE(B1, 1); ER_LOAD(B1, 3); ER_STORE(B0, 2); ER_LOAD(B0, 4); ER_STORE(B1, 3); ER_LOAD(B1, 5);
;         ER_STORE(B0, 4); ER_LOAD(B0, 6); ER_STORE(B1, 5); ER_LOAD(B1, 7); ER_STORE(B0, 6); ER_STORE(B1, 7);
	v_lshlrev_b32_e32 v144, 16, v28
	v_and_b32_e32 v145, 0xffff0000, v28
	v_lshlrev_b32_e32 v28, 16, v29
	v_and_b32_e32 v29, 0xffff0000, v29
	s_waitcnt vmcnt(8)
	v_lshlrev_b32_e32 v146, 16, v30
	v_and_b32_e32 v147, 0xffff0000, v30
	v_lshlrev_b32_e32 v148, 16, v31
	v_and_b32_e32 v149, 0xffff0000, v31
	v_lshl_add_u64 v[132:133], v[0:1], 0, s[20:21]
	v_pk_fma_f32 v[26:27], v[122:123], v[12:13], v[26:27]
	v_pk_fma_f32 v[30:31], v[118:119], v[8:9], v[28:29]
	v_pk_fma_f32 v[28:29], v[116:117], v[6:7], v[144:145]
	v_pk_fma_f32 v[114:115], v[114:115], v[4:5], v[148:149]
	v_pk_fma_f32 v[112:113], v[112:113], v[2:3], v[146:147]
	s_waitcnt vmcnt(2)
	v_lshlrev_b32_e32 v154, 16, v128
	v_lshlrev_b32_e32 v150, 16, v20
	v_and_b32_e32 v151, 0xffff0000, v20
	v_lshlrev_b32_e32 v152, 16, v21
	v_and_b32_e32 v153, 0xffff0000, v21
	s_waitcnt vmcnt(0)
	v_lshlrev_b32_e32 v158, 16, v22
	v_and_b32_e32 v159, 0xffff0000, v22
	v_lshlrev_b32_e32 v172, 16, v23
	v_and_b32_e32 v173, 0xffff0000, v23
	v_pk_fma_f32 v[22:23], v[126:127], v[14:15], v[24:25]
	v_pk_fma_f32 v[20:21], v[124:125], v[16:17], v[140:141]
	v_pk_fma_f32 v[24:25], v[120:121], v[10:11], v[142:143]
	global_store_dwordx4 v[134:135], v[20:23], off
	global_store_dwordx4 v[132:133], v[24:27], off offset:64
	global_store_dwordx4 v[132:133], v[28:31], off offset:512
	global_store_dwordx4 v[132:133], v[112:115], off offset:576
	v_pk_fma_f32 v[22:23], v[110:111], v[14:15], v[152:153]
	v_add_co_u32_e32 v110, vcc, s69, v0
	v_and_b32_e32 v155, 0xffff0000, v128
	v_lshlrev_b32_e32 v128, 16, v129
	v_and_b32_e32 v129, 0xffff0000, v129
	v_pk_fma_f32 v[20:21], v[108:109], v[16:17], v[150:151]
	v_addc_co_u32_e32 v111, vcc, 0, v1, vcc
	v_lshlrev_b32_e32 v156, 16, v130
	v_and_b32_e32 v157, 0xffff0000, v130
	v_lshlrev_b32_e32 v130, 16, v131
	v_and_b32_e32 v131, 0xffff0000, v131
	global_load_dwordx2 v[24:25], v[138:139], off
	global_load_dwordx2 v[26:27], v[136:137], off offset:32
	global_load_dwordx2 v[28:29], v[136:137], off offset:256
	global_load_dwordx2 v[30:31], v[136:137], off offset:288
	v_lshl_add_u64 v[108:109], v[0:1], 0, s[24:25]
	global_store_dwordx4 v[110:111], v[20:23], off
	s_waitcnt vmcnt(2)
	v_lshlrev_b32_e32 v110, 16, v28
	v_pk_fma_f32 v[22:23], v[106:107], v[12:13], v[128:129]
	v_pk_fma_f32 v[20:21], v[104:105], v[10:11], v[154:155]
	global_store_dwordx4 v[108:109], v[20:23], off offset:64
	v_lshlrev_b32_e32 v106, 16, v24
	v_and_b32_e32 v107, 0xffff0000, v24
	v_pk_fma_f32 v[22:23], v[102:103], v[8:9], v[130:131]
	v_pk_fma_f32 v[20:21], v[100:101], v[6:7], v[156:157]
	global_store_dwordx4 v[108:109], v[20:23], off offset:512
	v_lshlrev_b32_e32 v24, 16, v25
	v_and_b32_e32 v25, 0xffff0000, v25
	v_pk_fma_f32 v[22:23], v[98:99], v[4:5], v[172:173]
	v_pk_fma_f32 v[20:21], v[96:97], v[2:3], v[158:159]
	global_store_dwordx4 v[108:109], v[20:23], off offset:576
	v_lshlrev_b32_e32 v108, 16, v26
	v_and_b32_e32 v109, 0xffff0000, v26
	v_add_co_u32_e32 v20, vcc, s70, v18
	v_lshl_add_u64 v[22:23], v[18:19], 0, s[26:27]
	s_nop 0
	v_addc_co_u32_e32 v21, vcc, 0, v19, vcc
	global_load_dwordx2 v[20:21], v[20:21], off
	s_nop 0
	global_load_dwordx2 v[96:97], v[22:23], off offset:32
	global_load_dwordx2 v[98:99], v[22:23], off offset:256
	s_nop 0
	global_load_dwordx2 v[22:23], v[22:23], off offset:288
	v_add_co_u32_e32 v102, vcc, s71, v0
	v_lshlrev_b32_e32 v26, 16, v27
	s_nop 0
	v_addc_co_u32_e32 v103, vcc, 0, v1, vcc
	v_and_b32_e32 v27, 0xffff0000, v27
	v_and_b32_e32 v111, 0xffff0000, v28
	v_lshlrev_b32_e32 v28, 16, v29
	v_and_b32_e32 v29, 0xffff0000, v29
	s_waitcnt vmcnt(8)
	v_lshlrev_b32_e32 v112, 16, v30
	v_and_b32_e32 v113, 0xffff0000, v30
	v_lshlrev_b32_e32 v114, 16, v31
	v_and_b32_e32 v115, 0xffff0000, v31
	v_lshl_add_u64 v[100:101], v[0:1], 0, s[28:29]
	v_pk_fma_f32 v[26:27], v[90:91], v[12:13], v[26:27]
	v_pk_fma_f32 v[30:31], v[86:87], v[8:9], v[28:29]
	v_pk_fma_f32 v[28:29], v[84:85], v[6:7], v[110:111]
	v_pk_fma_f32 v[82:83], v[82:83], v[4:5], v[114:115]
	v_pk_fma_f32 v[80:81], v[80:81], v[2:3], v[112:113]
	v_lshl_add_u64 v[104:105], v[18:19], 0, s[30:31]
	s_waitcnt vmcnt(2)
	v_lshlrev_b32_e32 v120, 16, v96
	v_lshlrev_b32_e32 v116, 16, v20
	v_and_b32_e32 v117, 0xffff0000, v20
	v_lshlrev_b32_e32 v118, 16, v21
	v_and_b32_e32 v119, 0xffff0000, v21
	s_waitcnt vmcnt(0)
;     ...
;         if (!has_next) break;
;     __device__ __forceinline__ void operator()(const f32x4 (&acc)[2][2][4][2], const Unit& u, int wr, int wc, int fr, int fq) const {
;     ...
;         ER_LOAD(B0, 0); ER_LOAD(B1, 1); ER_STORE(B0, 0); ER_LOAD(B0, 2); ER_STORE(B1, 1); ER_LOAD(B1, 3); ER_STORE(B0, 2); ER_LOAD(B0, 4); ER_STORE(B1, 3); ER_LOAD(B1, 5);
;         ER_STORE(B0, 4); ER_LOAD(B0, 6); ER_STORE(B1, 5); ER_LOAD(B1, 7); ER_STORE(B0, 6); ER_STORE(B1, 7);
	v_lshlrev_b32_e32 v124, 16, v22
	v_and_b32_e32 v125, 0xffff0000, v22
	v_lshlrev_b32_e32 v126, 16, v23
	v_and_b32_e32 v127, 0xffff0000, v23
	v_pk_fma_f32 v[22:23], v[94:95], v[14:15], v[24:25]
	v_pk_fma_f32 v[20:21], v[92:93], v[16:17], v[106:107]
	v_pk_fma_f32 v[24:25], v[88:89], v[10:11], v[108:109]
	global_store_dwordx4 v[102:103], v[20:23], off
	global_store_dwordx4 v[100:101], v[24:27], off offset:64
	global_store_dwordx4 v[100:101], v[28:31], off offset:512
	global_store_dwordx4 v[100:101], v[80:83], off offset:576
	v_add_co_u32_e32 v20, vcc, s72, v18
	v_pk_fma_f32 v[22:23], v[78:79], v[14:15], v[118:119]
	s_nop 0
	v_addc_co_u32_e32 v21, vcc, 0, v19, vcc
	v_add_co_u32_e32 v78, vcc, s73, v0
	v_and_b32_e32 v121, 0xffff0000, v96
	v_lshlrev_b32_e32 v96, 16, v97
	v_and_b32_e32 v97, 0xffff0000, v97
	global_load_dwordx2 v[24:25], v[20:21], off
	global_load_dwordx2 v[26:27], v[104:105], off offset:32
	global_load_dwordx2 v[28:29], v[104:105], off offset:256
	global_load_dwordx2 v[30:31], v[104:105], off offset:288
	v_pk_fma_f32 v[20:21], v[76:77], v[16:17], v[116:117]
	v_addc_co_u32_e32 v79, vcc, 0, v1, vcc
	v_lshlrev_b32_e32 v122, 16, v98
	v_and_b32_e32 v123, 0xffff0000, v98
	v_lshlrev_b32_e32 v98, 16, v99
	v_and_b32_e32 v99, 0xffff0000, v99
	v_lshl_add_u64 v[76:77], v[0:1], 0, s[34:35]
	global_store_dwordx4 v[78:79], v[20:23], off
	s_waitcnt vmcnt(1)
	v_lshlrev_b32_e32 v78, 16, v30
	v_pk_fma_f32 v[22:23], v[74:75], v[12:13], v[96:97]
	v_pk_fma_f32 v[20:21], v[72:73], v[10:11], v[120:121]
	global_store_dwordx4 v[76:77], v[20:23], off offset:64
	v_lshlrev_b32_e32 v72, 16, v24
	v_and_b32_e32 v73, 0xffff0000, v24
	v_pk_fma_f32 v[22:23], v[70:71], v[8:9], v[98:99]
	v_pk_fma_f32 v[20:21], v[68:69], v[6:7], v[122:123]
	global_store_dwordx4 v[76:77], v[20:23], off offset:512
	v_lshl_add_u64 v[70:71], v[0:1], 0, s[40:41]
	v_lshlrev_b32_e32 v24, 16, v25
	v_pk_fma_f32 v[22:23], v[66:67], v[4:5], v[126:127]
	v_pk_fma_f32 v[20:21], v[64:65], v[2:3], v[124:125]
	global_store_dwordx4 v[76:77], v[20:23], off offset:576
	v_lshl_add_u64 v[66:67], v[0:1], 0, s[38:39]
	v_and_b32_e32 v25, 0xffff0000, v25
	v_add_co_u32_e32 v20, vcc, s74, v18
	v_lshlrev_b32_e32 v74, 16, v26
	s_nop 0
	v_addc_co_u32_e32 v21, vcc, 0, v19, vcc
	v_lshl_add_u64 v[18:19], v[18:19], 0, s[36:37]
	global_load_dwordx2 v[20:21], v[20:21], off
	s_nop 0
	global_load_dwordx2 v[22:23], v[18:19], off offset:32
	global_load_dwordx2 v[64:65], v[18:19], off offset:256
	s_nop 0
	global_load_dwordx2 v[18:19], v[18:19], off offset:288
	v_add_co_u32_e32 v68, vcc, s75, v0
	v_and_b32_e32 v75, 0xffff0000, v26
	s_nop 0
	v_addc_co_u32_e32 v69, vcc, 0, v1, vcc
	v_add_co_u32_e32 v0, vcc, s76, v0
	v_lshlrev_b32_e32 v26, 16, v27
	v_and_b32_e32 v27, 0xffff0000, v27
	v_lshlrev_b32_e32 v76, 16, v28
	v_and_b32_e32 v77, 0xffff0000, v28
	v_lshlrev_b32_e32 v28, 16, v29
	v_and_b32_e32 v29, 0xffff0000, v29
	v_and_b32_e32 v79, 0xffff0000, v30
	v_lshlrev_b32_e32 v30, 16, v31
	v_and_b32_e32 v31, 0xffff0000, v31
	v_addc_co_u32_e32 v1, vcc, 0, v1, vcc
	v_pk_fma_f32 v[28:29], v[50:51], v[8:9], v[28:29]
	v_pk_fma_f32 v[42:43], v[42:43], v[4:5], v[30:31]
	v_pk_fma_f32 v[40:41], v[40:41], v[2:3], v[78:79]
	s_and_b64 vcc, exec, s[0:1]
	s_mov_b64 s[0:1], -1
	s_waitcnt vmcnt(2)
	v_lshlrev_b32_e32 v84, 16, v22
	v_lshlrev_b32_e32 v80, 16, v20
	v_and_b32_e32 v81, 0xffff0000, v20
	v_lshlrev_b32_e32 v82, 16, v21
	v_and_b32_e32 v83, 0xffff0000, v21
	v_and_b32_e32 v85, 0xffff0000, v22
	v_lshlrev_b32_e32 v86, 16, v23
	v_and_b32_e32 v87, 0xffff0000, v23
	s_waitcnt vmcnt(1)
	v_lshlrev_b32_e32 v88, 16, v64
	v_and_b32_e32 v89, 0xffff0000, v64
	v_lshlrev_b32_e32 v64, 16, v65
	v_and_b32_e32 v65, 0xffff0000, v65
	s_waitcnt vmcnt(0)
	v_lshlrev_b32_e32 v90, 16, v18
	v_and_b32_e32 v91, 0xffff0000, v18
	v_lshlrev_b32_e32 v92, 16, v19
	v_and_b32_e32 v93, 0xffff0000, v19
	v_pk_fma_f32 v[20:21], v[62:63], v[14:15], v[24:25]
	v_pk_fma_f32 v[18:19], v[60:61], v[16:17], v[72:73]
	v_pk_fma_f32 v[24:25], v[58:59], v[12:13], v[26:27]
	v_pk_fma_f32 v[22:23], v[56:57], v[10:11], v[74:75]
	v_pk_fma_f32 v[26:27], v[48:49], v[6:7], v[76:77]
	global_store_dwordx4 v[68:69], v[18:21], off
	global_store_dwordx4 v[66:67], v[22:25], off offset:64
	global_store_dwordx4 v[66:67], v[26:29], off offset:512
	global_store_dwordx4 v[66:67], v[40:43], off offset:576
	v_pk_fma_f32 v[18:19], v[54:55], v[14:15], v[82:83]
	v_pk_fma_f32 v[16:17], v[52:53], v[16:17], v[80:81]
	v_pk_fma_f32 v[12:13], v[46:47], v[12:13], v[86:87]
	v_pk_fma_f32 v[10:11], v[44:45], v[10:11], v[84:85]
	v_pk_fma_f32 v[8:9], v[38:39], v[8:9], v[64:65]
	v_pk_fma_f32 v[6:7], v[36:37], v[6:7], v[88:89]
	v_pk_fma_f32 v[4:5], v[34:35], v[4:5], v[92:93]
	v_pk_fma_f32 v[2:3], v[32:33], v[2:3], v[90:91]
	global_store_dwordx4 v[0:1], v[16:19], off
	global_store_dwordx4 v[70:71], v[10:13], off offset:64
	global_store_dwordx4 v[70:71], v[6:9], off offset:512
	global_store_dwordx4 v[70:71], v[2:5], off offset:576
	s_cbranch_vccnz .LBB0_2636
	s_andn2_b64 vcc, exec, s[6:7]
	s_cbranch_vccnz .LBB0_2635
	s_barrier
	s_branch .LBB0_2635
